# E1 on bf16 MFMA 16x16x32: table rows gathered coalesced by LDS-DMA into a per-wave 16 KiB ring, read back swizzled in operand layout, fp4->bf16 exact, f32 accumulate
# speedup vs baseline: 1.0689x; 1.0110x over previous
.Le1w_first:
	s_mov_b64 exec, 1
	global_atomic_add v250, v211, v1, s[0:1] sc0
	s_mov_b64 exec, -1
	v_mov_b32_e32 v249, 0x80
	v_and_b32_e32 v233, 7, v0
	v_bfe_u32 v234, v0, 4, 2
	v_xor_b32_e32 v235, v233, v234
	v_lshlrev_b32_e32 v144, 4, v235
	v_xor_b32_e32 v145, 64, v144
	v_and_b32_e32 v233, 15, v0
	v_bfe_u32 v234, v0, 4, 2
	v_bfe_u32 v235, v0, 1, 3
	v_xor_b32_e32 v235, v234, v235
	v_lshlrev_b32_e32 v235, 4, v235
	v_lshl_add_u32 v235, v233, 7, v235
	v_lshrrev_b32_e32 v236, 6, v0
	s_nop 0
	v_readfirstlane_b32 s38, v236
	s_lshl_b32 s38, s38, 14
	v_add_u32_e32 v146, s38, v235
	v_xor_b32_e32 v147, 64, v146
	s_add_u32 s2, s96, 0x4c00000
	s_addc_u32 s3, s97, 0
	s_add_u32 s4, s96, 0x27600000
	s_addc_u32 s5, s97, 0
	s_add_u32 s4, s4, s80
	s_addc_u32 s5, s5, 0
	s_lshl_b32 s33, s60, 3
	s_waitcnt vmcnt(0)
	v_readfirstlane_b32 s35, v250
	s_cmp_ge_i32 s35, s33
	s_cbranch_scc1 .LBB0_722
	s_lshr_b32 s99, s35, 3
	s_lshl_b32 s98, s99, 6
	s_and_b32 s99, s99, 0xffffff00
	s_add_i32 s99, s99, 0x100
	s_and_b64 s[24:25], s[30:31], exec
	s_cselect_b32 s99, 0, s99
	s_add_i32 s98, s98, s99
	s_and_b32 s99, s35, 7
	s_lshl_b32 s99, s99, 3
	s_add_i32 s98, s98, s99
	s_mov_b32 s39, s98
	v_bfe_u32 v234, v0, 3, 3
	s_lshl_b32 s99, s98, 8
	v_lshl_add_u32 v149, v234, 5, s99
	v_and_b32_e32 v233, 7, v0
	v_lshl_add_u32 v233, v233, 5, s99
	v_bfe_u32 v235, v0, 3, 1
	v_lshl_add_u32 v151, v235, 4, v233
	s_lshl_b32 s99, s98, 12
	s_add_i32 s99, s99, s76
	v_bfe_u32 v234, v0, 4, 2
	v_lshl_add_u32 v150, v234, 6, s99
	global_load_dwordx4 v[66:69], v149, s[22:23]
	global_load_dwordx4 v[70:73], v149, s[22:23] offset:16
	v_add_u32_e32 v149, 0x100, v149
	global_load_dwordx4 v[74:77], v149, s[22:23]
	global_load_dwordx4 v[78:81], v149, s[22:23] offset:16
	v_add_u32_e32 v149, 0x100, v149
	global_load_dwordx4 v[2:5], v150, s[2:3]
	global_load_dwordx4 v[6:9], v150, s[2:3] offset:16
	global_load_dwordx4 v[10:13], v150, s[2:3] offset:32
	global_load_dwordx4 v[14:17], v150, s[2:3] offset:48
	global_load_dwordx4 v[18:21], v150, s[2:3] offset:256
	global_load_dwordx4 v[22:25], v150, s[2:3] offset:272
	global_load_dwordx4 v[26:29], v150, s[2:3] offset:288
	global_load_dwordx4 v[30:33], v150, s[2:3] offset:304
	v_add_u32_e32 v150, 0x1000, v150
	s_waitcnt vmcnt(10)
	s_add_i32 m0, s38, 0x0
	v_mad_u32_u16 v142, v66, v249, v144
	global_load_lds_dwordx4 v142, s[10:11]
	s_add_i32 m0, s38, 0x400
	v_mad_u32_u16 v143, v70, v249, v145
	global_load_lds_dwordx4 v143, s[10:11]
	s_add_i32 m0, s38, 0x800
	v_mad_u32_u16 v142, v66, v249, v144 op_sel:[1,0,0,0]
	global_load_lds_dwordx4 v142, s[10:11]
	s_add_i32 m0, s38, 0xc00
	v_mad_u32_u16 v143, v70, v249, v145 op_sel:[1,0,0,0]
	global_load_lds_dwordx4 v143, s[10:11]
	s_add_i32 m0, s38, 0x1000
	v_mad_u32_u16 v142, v67, v249, v144
	global_load_lds_dwordx4 v142, s[10:11]
	s_add_i32 m0, s38, 0x1400
	v_mad_u32_u16 v143, v71, v249, v145
	global_load_lds_dwordx4 v143, s[10:11]
	s_add_i32 m0, s38, 0x1800
	v_mad_u32_u16 v142, v67, v249, v144 op_sel:[1,0,0,0]
	global_load_lds_dwordx4 v142, s[10:11]
	s_add_i32 m0, s38, 0x1c00
	v_mad_u32_u16 v143, v71, v249, v145 op_sel:[1,0,0,0]
	global_load_lds_dwordx4 v143, s[10:11]
	s_add_i32 m0, s38, 0x2000
	v_mad_u32_u16 v142, v68, v249, v144
	global_load_lds_dwordx4 v142, s[10:11]
	s_add_i32 m0, s38, 0x2400
	v_mad_u32_u16 v143, v72, v249, v145
	global_load_lds_dwordx4 v143, s[10:11]
	s_add_i32 m0, s38, 0x2800
	v_mad_u32_u16 v142, v68, v249, v144 op_sel:[1,0,0,0]
	global_load_lds_dwordx4 v142, s[10:11]
	s_add_i32 m0, s38, 0x2c00
	v_mad_u32_u16 v143, v72, v249, v145 op_sel:[1,0,0,0]
	global_load_lds_dwordx4 v143, s[10:11]
	s_add_i32 m0, s38, 0x3000
	v_mad_u32_u16 v142, v69, v249, v144
	global_load_lds_dwordx4 v142, s[10:11]
	s_add_i32 m0, s38, 0x3400
	v_mad_u32_u16 v143, v73, v249, v145
	global_load_lds_dwordx4 v143, s[10:11]
	s_add_i32 m0, s38, 0x3800
	v_mad_u32_u16 v142, v69, v249, v144 op_sel:[1,0,0,0]
	global_load_lds_dwordx4 v142, s[10:11]
	s_add_i32 m0, s38, 0x3c00
	v_mad_u32_u16 v143, v73, v249, v145 op_sel:[1,0,0,0]
	global_load_lds_dwordx4 v143, s[10:11]
	s_mov_b32 s34, 0
	s_mov_b32 s43, 0
	s_waitcnt vmcnt(0)
	ds_read_b128 v[82:85], v146
	ds_read_b128 v[86:89], v147
.Le1_loop:
	s_movk_i32 s40, 0x1000
	s_movk_i32 s41, 0x100
	s_movk_i32 s42, 0x100
	s_cmp_eq_u32 s34, 2
	s_cbranch_scc0 .Le1_noatom
	s_mov_b64 exec, 1
	global_atomic_add v250, v211, v1, s[0:1] sc0
	s_mov_b64 exec, -1
.Le1_noatom:
	s_cmp_eq_u32 s34, 4
	s_cbranch_scc0 .Le1_noprep
	v_readfirstlane_b32 s35, v250
	s_mov_b32 s43, -7
	s_cmp_ge_i32 s35, s33
	s_cbranch_scc1 .Le1_nonext
	s_lshr_b32 s99, s35, 3
	s_lshl_b32 s98, s99, 6
	s_and_b32 s99, s99, 0xffffff00
	s_add_i32 s99, s99, 0x100
	s_and_b64 s[24:25], s[30:31], exec
	s_cselect_b32 s99, 0, s99
	s_add_i32 s98, s98, s99
	s_and_b32 s99, s35, 7
	s_lshl_b32 s99, s99, 3
	s_add_i32 s98, s98, s99
	s_sub_i32 s43, s98, s39
	s_add_i32 s43, s43, -7
	s_branch .Le1_prepdone

.Le1_prepdone:
	s_lshl_b32 s41, s43, 8
.Le1_noprep:
	s_cmp_eq_u32 s34, 6
	s_cbranch_scc0 .Le1_no6
	s_lshl_b32 s40, s43, 12
	s_lshl_b32 s42, s43, 8
.Le1_no6:
	global_load_dwordx4 v[34:37], v150, s[2:3]
	global_load_dwordx4 v[38:41], v150, s[2:3] offset:16
	global_load_dwordx4 v[42:45], v150, s[2:3] offset:32
	global_load_dwordx4 v[46:49], v150, s[2:3] offset:48
	global_load_dwordx4 v[50:53], v150, s[2:3] offset:256
	global_load_dwordx4 v[54:57], v150, s[2:3] offset:272
	global_load_dwordx4 v[58:61], v150, s[2:3] offset:288
	global_load_dwordx4 v[62:65], v150, s[2:3] offset:304
	v_add_u32_e32 v150, s40, v150
	global_load_dwordx4 v[66:69], v149, s[22:23]
	global_load_dwordx4 v[70:73], v149, s[22:23] offset:16
	v_add_u32_e32 v149, 0x100, v149
	s_waitcnt vmcnt(23)
	ds_read_b128 v[90:93], v146 offset:2048
	ds_read_b128 v[94:97], v147 offset:2048
	s_waitcnt lgkmcnt(2)
	s_add_i32 m0, s38, 0x0
	v_mad_u32_u16 v142, v74, v249, v144
	global_load_lds_dwordx4 v142, s[10:11]
	s_add_i32 m0, s38, 0x400
	v_mad_u32_u16 v143, v78, v249, v145
	global_load_lds_dwordx4 v143, s[10:11]
	v_cvt_scalef32_pk_bf16_fp4 v98, v82, 1.0
	v_cvt_scalef32_pk_bf16_fp4 v99, v82, 1.0 op_sel:[1,0,0]
	v_cvt_scalef32_pk_bf16_fp4 v100, v82, 1.0 op_sel:[0,1,0]
	v_cvt_scalef32_pk_bf16_fp4 v101, v82, 1.0 op_sel:[1,1,0]
	v_cvt_scalef32_pk_bf16_fp4 v102, v83, 1.0
	v_cvt_scalef32_pk_bf16_fp4 v103, v83, 1.0 op_sel:[1,0,0]
	v_cvt_scalef32_pk_bf16_fp4 v104, v83, 1.0 op_sel:[0,1,0]
	v_cvt_scalef32_pk_bf16_fp4 v105, v83, 1.0 op_sel:[1,1,0]
	v_mfma_f32_16x16x32_bf16 v[106:109], v[2:5], v[98:101], 0
	v_cvt_scalef32_pk_bf16_fp4 v98, v84, 1.0
	v_cvt_scalef32_pk_bf16_fp4 v99, v84, 1.0 op_sel:[1,0,0]
	v_cvt_scalef32_pk_bf16_fp4 v100, v84, 1.0 op_sel:[0,1,0]
	v_cvt_scalef32_pk_bf16_fp4 v101, v84, 1.0 op_sel:[1,1,0]
	v_mfma_f32_16x16x32_bf16 v[106:109], v[6:9], v[102:105], v[106:109]
	v_cvt_scalef32_pk_bf16_fp4 v102, v85, 1.0
	v_cvt_scalef32_pk_bf16_fp4 v103, v85, 1.0 op_sel:[1,0,0]
	v_cvt_scalef32_pk_bf16_fp4 v104, v85, 1.0 op_sel:[0,1,0]
	v_cvt_scalef32_pk_bf16_fp4 v105, v85, 1.0 op_sel:[1,1,0]
	v_mfma_f32_16x16x32_bf16 v[106:109], v[10:13], v[98:101], v[106:109]
	v_cvt_scalef32_pk_bf16_fp4 v98, v86, 1.0
	v_cvt_scalef32_pk_bf16_fp4 v99, v86, 1.0 op_sel:[1,0,0]
	v_cvt_scalef32_pk_bf16_fp4 v100, v86, 1.0 op_sel:[0,1,0]
	v_cvt_scalef32_pk_bf16_fp4 v101, v86, 1.0 op_sel:[1,1,0]
	v_mfma_f32_16x16x32_bf16 v[106:109], v[14:17], v[102:105], v[106:109]
	v_cvt_scalef32_pk_bf16_fp4 v102, v87, 1.0
	v_cvt_scalef32_pk_bf16_fp4 v103, v87, 1.0 op_sel:[1,0,0]
	v_cvt_scalef32_pk_bf16_fp4 v104, v87, 1.0 op_sel:[0,1,0]
	v_cvt_scalef32_pk_bf16_fp4 v105, v87, 1.0 op_sel:[1,1,0]
	v_mfma_f32_16x16x32_bf16 v[106:109], v[18:21], v[98:101], v[106:109]
	v_cvt_scalef32_pk_bf16_fp4 v98, v88, 1.0
	v_cvt_scalef32_pk_bf16_fp4 v99, v88, 1.0 op_sel:[1,0,0]
	v_cvt_scalef32_pk_bf16_fp4 v100, v88, 1.0 op_sel:[0,1,0]
	v_cvt_scalef32_pk_bf16_fp4 v101, v88, 1.0 op_sel:[1,1,0]
	v_mfma_f32_16x16x32_bf16 v[106:109], v[22:25], v[102:105], v[106:109]
	v_cvt_scalef32_pk_bf16_fp4 v102, v89, 1.0
	v_cvt_scalef32_pk_bf16_fp4 v103, v89, 1.0 op_sel:[1,0,0]
	v_cvt_scalef32_pk_bf16_fp4 v104, v89, 1.0 op_sel:[0,1,0]
	v_cvt_scalef32_pk_bf16_fp4 v105, v89, 1.0 op_sel:[1,1,0]
	v_mfma_f32_16x16x32_bf16 v[106:109], v[26:29], v[98:101], v[106:109]
	v_mfma_f32_16x16x32_bf16 v[106:109], v[30:33], v[102:105], v[106:109]
	s_waitcnt vmcnt(23)
	ds_read_b128 v[82:85], v146 offset:4096
	ds_read_b128 v[86:89], v147 offset:4096
	s_waitcnt lgkmcnt(2)
	s_add_i32 m0, s38, 0x800
	v_mad_u32_u16 v142, v74, v249, v144 op_sel:[1,0,0,0]
	global_load_lds_dwordx4 v142, s[10:11]
	s_add_i32 m0, s38, 0xc00
	v_mad_u32_u16 v143, v78, v249, v145 op_sel:[1,0,0,0]
	global_load_lds_dwordx4 v143, s[10:11]
	v_cvt_scalef32_pk_bf16_fp4 v98, v90, 1.0
	v_cvt_scalef32_pk_bf16_fp4 v99, v90, 1.0 op_sel:[1,0,0]
	v_cvt_scalef32_pk_bf16_fp4 v100, v90, 1.0 op_sel:[0,1,0]
	v_cvt_scalef32_pk_bf16_fp4 v101, v90, 1.0 op_sel:[1,1,0]
	v_cvt_scalef32_pk_bf16_fp4 v102, v91, 1.0
	v_cvt_scalef32_pk_bf16_fp4 v103, v91, 1.0 op_sel:[1,0,0]
	v_cvt_scalef32_pk_bf16_fp4 v104, v91, 1.0 op_sel:[0,1,0]
	v_cvt_scalef32_pk_bf16_fp4 v105, v91, 1.0 op_sel:[1,1,0]
	v_mfma_f32_16x16x32_bf16 v[110:113], v[2:5], v[98:101], 0
	v_cvt_scalef32_pk_bf16_fp4 v98, v92, 1.0
	v_cvt_scalef32_pk_bf16_fp4 v99, v92, 1.0 op_sel:[1,0,0]
	v_cvt_scalef32_pk_bf16_fp4 v100, v92, 1.0 op_sel:[0,1,0]
	v_cvt_scalef32_pk_bf16_fp4 v101, v92, 1.0 op_sel:[1,1,0]
	v_mfma_f32_16x16x32_bf16 v[110:113], v[6:9], v[102:105], v[110:113]
	v_cvt_scalef32_pk_bf16_fp4 v102, v93, 1.0
	v_cvt_scalef32_pk_bf16_fp4 v103, v93, 1.0 op_sel:[1,0,0]
	v_cvt_scalef32_pk_bf16_fp4 v104, v93, 1.0 op_sel:[0,1,0]
	v_cvt_scalef32_pk_bf16_fp4 v105, v93, 1.0 op_sel:[1,1,0]
	v_mfma_f32_16x16x32_bf16 v[110:113], v[10:13], v[98:101], v[110:113]
	v_cvt_scalef32_pk_bf16_fp4 v98, v94, 1.0
	v_cvt_scalef32_pk_bf16_fp4 v99, v94, 1.0 op_sel:[1,0,0]
	v_cvt_scalef32_pk_bf16_fp4 v100, v94, 1.0 op_sel:[0,1,0]
	v_cvt_scalef32_pk_bf16_fp4 v101, v94, 1.0 op_sel:[1,1,0]
	v_mfma_f32_16x16x32_bf16 v[110:113], v[14:17], v[102:105], v[110:113]
	v_cvt_scalef32_pk_bf16_fp4 v102, v95, 1.0
	v_cvt_scalef32_pk_bf16_fp4 v103, v95, 1.0 op_sel:[1,0,0]
	v_cvt_scalef32_pk_bf16_fp4 v104, v95, 1.0 op_sel:[0,1,0]
	v_cvt_scalef32_pk_bf16_fp4 v105, v95, 1.0 op_sel:[1,1,0]
	v_mfma_f32_16x16x32_bf16 v[110:113], v[18:21], v[98:101], v[110:113]
	v_cvt_scalef32_pk_bf16_fp4 v98, v96, 1.0
	v_cvt_scalef32_pk_bf16_fp4 v99, v96, 1.0 op_sel:[1,0,0]
	v_cvt_scalef32_pk_bf16_fp4 v100, v96, 1.0 op_sel:[0,1,0]
	v_cvt_scalef32_pk_bf16_fp4 v101, v96, 1.0 op_sel:[1,1,0]
	v_mfma_f32_16x16x32_bf16 v[110:113], v[22:25], v[102:105], v[110:113]
	v_cvt_scalef32_pk_bf16_fp4 v102, v97, 1.0
	v_cvt_scalef32_pk_bf16_fp4 v103, v97, 1.0 op_sel:[1,0,0]
	v_cvt_scalef32_pk_bf16_fp4 v104, v97, 1.0 op_sel:[0,1,0]
	v_cvt_scalef32_pk_bf16_fp4 v105, v97, 1.0 op_sel:[1,1,0]
	v_mfma_f32_16x16x32_bf16 v[110:113], v[26:29], v[98:101], v[110:113]
	v_mfma_f32_16x16x32_bf16 v[110:113], v[30:33], v[102:105], v[110:113]
	s_waitcnt vmcnt(23)
	ds_read_b128 v[90:93], v146 offset:6144
	ds_read_b128 v[94:97], v147 offset:6144
	s_waitcnt lgkmcnt(2)
	s_add_i32 m0, s38, 0x1000
	v_mad_u32_u16 v142, v75, v249, v144
	global_load_lds_dwordx4 v142, s[10:11]
	s_add_i32 m0, s38, 0x1400
	v_mad_u32_u16 v143, v79, v249, v145
	global_load_lds_dwordx4 v143, s[10:11]
	v_cvt_scalef32_pk_bf16_fp4 v98, v82, 1.0
	v_cvt_scalef32_pk_bf16_fp4 v99, v82, 1.0 op_sel:[1,0,0]
	v_cvt_scalef32_pk_bf16_fp4 v100, v82, 1.0 op_sel:[0,1,0]
	v_cvt_scalef32_pk_bf16_fp4 v101, v82, 1.0 op_sel:[1,1,0]
	v_cvt_scalef32_pk_bf16_fp4 v102, v83, 1.0
	v_cvt_scalef32_pk_bf16_fp4 v103, v83, 1.0 op_sel:[1,0,0]
	v_cvt_scalef32_pk_bf16_fp4 v104, v83, 1.0 op_sel:[0,1,0]
	v_cvt_scalef32_pk_bf16_fp4 v105, v83, 1.0 op_sel:[1,1,0]
	v_mfma_f32_16x16x32_bf16 v[114:117], v[2:5], v[98:101], 0
	v_cvt_scalef32_pk_bf16_fp4 v98, v84, 1.0
	v_cvt_scalef32_pk_bf16_fp4 v99, v84, 1.0 op_sel:[1,0,0]
	v_cvt_scalef32_pk_bf16_fp4 v100, v84, 1.0 op_sel:[0,1,0]
	v_cvt_scalef32_pk_bf16_fp4 v101, v84, 1.0 op_sel:[1,1,0]
	v_mfma_f32_16x16x32_bf16 v[114:117], v[6:9], v[102:105], v[114:117]
	v_cvt_scalef32_pk_bf16_fp4 v102, v85, 1.0
	v_cvt_scalef32_pk_bf16_fp4 v103, v85, 1.0 op_sel:[1,0,0]
	v_cvt_scalef32_pk_bf16_fp4 v104, v85, 1.0 op_sel:[0,1,0]
	v_cvt_scalef32_pk_bf16_fp4 v105, v85, 1.0 op_sel:[1,1,0]
	v_mfma_f32_16x16x32_bf16 v[114:117], v[10:13], v[98:101], v[114:117]
	v_cvt_scalef32_pk_bf16_fp4 v98, v86, 1.0
	v_cvt_scalef32_pk_bf16_fp4 v99, v86, 1.0 op_sel:[1,0,0]
	v_cvt_scalef32_pk_bf16_fp4 v100, v86, 1.0 op_sel:[0,1,0]
	v_cvt_scalef32_pk_bf16_fp4 v101, v86, 1.0 op_sel:[1,1,0]
	v_mfma_f32_16x16x32_bf16 v[114:117], v[14:17], v[102:105], v[114:117]
	v_cvt_scalef32_pk_bf16_fp4 v102, v87, 1.0
	v_cvt_scalef32_pk_bf16_fp4 v103, v87, 1.0 op_sel:[1,0,0]
	v_cvt_scalef32_pk_bf16_fp4 v104, v87, 1.0 op_sel:[0,1,0]
	v_cvt_scalef32_pk_bf16_fp4 v105, v87, 1.0 op_sel:[1,1,0]
	v_mfma_f32_16x16x32_bf16 v[114:117], v[18:21], v[98:101], v[114:117]
	v_cvt_scalef32_pk_bf16_fp4 v98, v88, 1.0
	v_cvt_scalef32_pk_bf16_fp4 v99, v88, 1.0 op_sel:[1,0,0]
	v_cvt_scalef32_pk_bf16_fp4 v100, v88, 1.0 op_sel:[0,1,0]
	v_cvt_scalef32_pk_bf16_fp4 v101, v88, 1.0 op_sel:[1,1,0]
	v_mfma_f32_16x16x32_bf16 v[114:117], v[22:25], v[102:105], v[114:117]
	v_cvt_scalef32_pk_bf16_fp4 v102, v89, 1.0
	v_cvt_scalef32_pk_bf16_fp4 v103, v89, 1.0 op_sel:[1,0,0]
	v_cvt_scalef32_pk_bf16_fp4 v104, v89, 1.0 op_sel:[0,1,0]
	v_cvt_scalef32_pk_bf16_fp4 v105, v89, 1.0 op_sel:[1,1,0]
	v_mfma_f32_16x16x32_bf16 v[114:117], v[26:29], v[98:101], v[114:117]
	v_mfma_f32_16x16x32_bf16 v[114:117], v[30:33], v[102:105], v[114:117]
	s_waitcnt vmcnt(23)
	ds_read_b128 v[82:85], v146 offset:8192
	ds_read_b128 v[86:89], v147 offset:8192
	s_waitcnt lgkmcnt(2)
	s_add_i32 m0, s38, 0x1800
	v_mad_u32_u16 v142, v75, v249, v144 op_sel:[1,0,0,0]
	global_load_lds_dwordx4 v142, s[10:11]
	s_add_i32 m0, s38, 0x1c00
	v_mad_u32_u16 v143, v79, v249, v145 op_sel:[1,0,0,0]
	global_load_lds_dwordx4 v143, s[10:11]
	v_cvt_scalef32_pk_bf16_fp4 v98, v90, 1.0
	v_cvt_scalef32_pk_bf16_fp4 v99, v90, 1.0 op_sel:[1,0,0]
	v_cvt_scalef32_pk_bf16_fp4 v100, v90, 1.0 op_sel:[0,1,0]
	v_cvt_scalef32_pk_bf16_fp4 v101, v90, 1.0 op_sel:[1,1,0]
	v_cvt_scalef32_pk_bf16_fp4 v102, v91, 1.0
	v_cvt_scalef32_pk_bf16_fp4 v103, v91, 1.0 op_sel:[1,0,0]
	v_cvt_scalef32_pk_bf16_fp4 v104, v91, 1.0 op_sel:[0,1,0]
	v_cvt_scalef32_pk_bf16_fp4 v105, v91, 1.0 op_sel:[1,1,0]
	v_mfma_f32_16x16x32_bf16 v[118:121], v[2:5], v[98:101], 0
	v_cvt_scalef32_pk_bf16_fp4 v98, v92, 1.0
	v_cvt_scalef32_pk_bf16_fp4 v99, v92, 1.0 op_sel:[1,0,0]
	v_cvt_scalef32_pk_bf16_fp4 v100, v92, 1.0 op_sel:[0,1,0]
	v_cvt_scalef32_pk_bf16_fp4 v101, v92, 1.0 op_sel:[1,1,0]
	v_mfma_f32_16x16x32_bf16 v[118:121], v[6:9], v[102:105], v[118:121]
	v_cvt_scalef32_pk_bf16_fp4 v102, v93, 1.0
	v_cvt_scalef32_pk_bf16_fp4 v103, v93, 1.0 op_sel:[1,0,0]
	v_cvt_scalef32_pk_bf16_fp4 v104, v93, 1.0 op_sel:[0,1,0]
	v_cvt_scalef32_pk_bf16_fp4 v105, v93, 1.0 op_sel:[1,1,0]
	v_mfma_f32_16x16x32_bf16 v[118:121], v[10:13], v[98:101], v[118:121]
	v_cvt_scalef32_pk_bf16_fp4 v98, v94, 1.0
	v_cvt_scalef32_pk_bf16_fp4 v99, v94, 1.0 op_sel:[1,0,0]
	v_cvt_scalef32_pk_bf16_fp4 v100, v94, 1.0 op_sel:[0,1,0]
	v_cvt_scalef32_pk_bf16_fp4 v101, v94, 1.0 op_sel:[1,1,0]
	v_mfma_f32_16x16x32_bf16 v[118:121], v[14:17], v[102:105], v[118:121]
	v_cvt_scalef32_pk_bf16_fp4 v102, v95, 1.0
	v_cvt_scalef32_pk_bf16_fp4 v103, v95, 1.0 op_sel:[1,0,0]
	v_cvt_scalef32_pk_bf16_fp4 v104, v95, 1.0 op_sel:[0,1,0]
	v_cvt_scalef32_pk_bf16_fp4 v105, v95, 1.0 op_sel:[1,1,0]
	v_mfma_f32_16x16x32_bf16 v[118:121], v[18:21], v[98:101], v[118:121]
	v_cvt_scalef32_pk_bf16_fp4 v98, v96, 1.0
	v_cvt_scalef32_pk_bf16_fp4 v99, v96, 1.0 op_sel:[1,0,0]
	v_cvt_scalef32_pk_bf16_fp4 v100, v96, 1.0 op_sel:[0,1,0]
	v_cvt_scalef32_pk_bf16_fp4 v101, v96, 1.0 op_sel:[1,1,0]
	v_mfma_f32_16x16x32_bf16 v[118:121], v[22:25], v[102:105], v[118:121]
	v_cvt_scalef32_pk_bf16_fp4 v102, v97, 1.0
	v_cvt_scalef32_pk_bf16_fp4 v103, v97, 1.0 op_sel:[1,0,0]
	v_cvt_scalef32_pk_bf16_fp4 v104, v97, 1.0 op_sel:[0,1,0]
	v_cvt_scalef32_pk_bf16_fp4 v105, v97, 1.0 op_sel:[1,1,0]
	v_mfma_f32_16x16x32_bf16 v[118:121], v[26:29], v[98:101], v[118:121]
	v_cvt_pk_bf16_f32 v138, v106, v110
	v_mfma_f32_16x16x32_bf16 v[118:121], v[30:33], v[102:105], v[118:121]
	s_waitcnt vmcnt(23)
	ds_read_b128 v[90:93], v146 offset:10240
	ds_read_b128 v[94:97], v147 offset:10240
	s_waitcnt lgkmcnt(2)
	s_add_i32 m0, s38, 0x2000
	v_mad_u32_u16 v142, v76, v249, v144
	global_load_lds_dwordx4 v142, s[10:11]
	s_add_i32 m0, s38, 0x2400
	v_mad_u32_u16 v143, v80, v249, v145
	global_load_lds_dwordx4 v143, s[10:11]
	v_cvt_scalef32_pk_bf16_fp4 v98, v82, 1.0
	v_cvt_scalef32_pk_bf16_fp4 v99, v82, 1.0 op_sel:[1,0,0]
	v_cvt_scalef32_pk_bf16_fp4 v100, v82, 1.0 op_sel:[0,1,0]
	v_cvt_scalef32_pk_bf16_fp4 v101, v82, 1.0 op_sel:[1,1,0]
	v_cvt_scalef32_pk_bf16_fp4 v102, v83, 1.0
	v_cvt_scalef32_pk_bf16_fp4 v103, v83, 1.0 op_sel:[1,0,0]
	v_cvt_scalef32_pk_bf16_fp4 v104, v83, 1.0 op_sel:[0,1,0]
	v_cvt_scalef32_pk_bf16_fp4 v105, v83, 1.0 op_sel:[1,1,0]
	v_mfma_f32_16x16x32_bf16 v[122:125], v[2:5], v[98:101], 0
	v_cvt_scalef32_pk_bf16_fp4 v98, v84, 1.0
	v_cvt_scalef32_pk_bf16_fp4 v99, v84, 1.0 op_sel:[1,0,0]
	v_cvt_scalef32_pk_bf16_fp4 v100, v84, 1.0 op_sel:[0,1,0]
	v_cvt_scalef32_pk_bf16_fp4 v101, v84, 1.0 op_sel:[1,1,0]
	v_mfma_f32_16x16x32_bf16 v[122:125], v[6:9], v[102:105], v[122:125]
	v_cvt_scalef32_pk_bf16_fp4 v102, v85, 1.0
	v_cvt_scalef32_pk_bf16_fp4 v103, v85, 1.0 op_sel:[1,0,0]
	v_cvt_scalef32_pk_bf16_fp4 v104, v85, 1.0 op_sel:[0,1,0]
	v_cvt_scalef32_pk_bf16_fp4 v105, v85, 1.0 op_sel:[1,1,0]
	v_mfma_f32_16x16x32_bf16 v[122:125], v[10:13], v[98:101], v[122:125]
	v_cvt_scalef32_pk_bf16_fp4 v98, v86, 1.0
	v_cvt_scalef32_pk_bf16_fp4 v99, v86, 1.0 op_sel:[1,0,0]
	v_cvt_scalef32_pk_bf16_fp4 v100, v86, 1.0 op_sel:[0,1,0]
	v_cvt_scalef32_pk_bf16_fp4 v101, v86, 1.0 op_sel:[1,1,0]
	v_mfma_f32_16x16x32_bf16 v[122:125], v[14:17], v[102:105], v[122:125]
	v_cvt_scalef32_pk_bf16_fp4 v102, v87, 1.0
	v_cvt_scalef32_pk_bf16_fp4 v103, v87, 1.0 op_sel:[1,0,0]
	v_cvt_scalef32_pk_bf16_fp4 v104, v87, 1.0 op_sel:[0,1,0]
	v_cvt_scalef32_pk_bf16_fp4 v105, v87, 1.0 op_sel:[1,1,0]
	v_mfma_f32_16x16x32_bf16 v[122:125], v[18:21], v[98:101], v[122:125]
	v_cvt_scalef32_pk_bf16_fp4 v98, v88, 1.0
	v_cvt_scalef32_pk_bf16_fp4 v99, v88, 1.0 op_sel:[1,0,0]
	v_cvt_scalef32_pk_bf16_fp4 v100, v88, 1.0 op_sel:[0,1,0]
	v_cvt_scalef32_pk_bf16_fp4 v101, v88, 1.0 op_sel:[1,1,0]
	v_mfma_f32_16x16x32_bf16 v[122:125], v[22:25], v[102:105], v[122:125]
	v_cvt_scalef32_pk_bf16_fp4 v102, v89, 1.0
	v_cvt_scalef32_pk_bf16_fp4 v103, v89, 1.0 op_sel:[1,0,0]
	v_cvt_scalef32_pk_bf16_fp4 v104, v89, 1.0 op_sel:[0,1,0]
	v_cvt_scalef32_pk_bf16_fp4 v105, v89, 1.0 op_sel:[1,1,0]
	v_mfma_f32_16x16x32_bf16 v[122:125], v[26:29], v[98:101], v[122:125]
	v_mfma_f32_16x16x32_bf16 v[122:125], v[30:33], v[102:105], v[122:125]
	s_waitcnt vmcnt(23)
	ds_read_b128 v[82:85], v146 offset:12288
	ds_read_b128 v[86:89], v147 offset:12288
	s_waitcnt lgkmcnt(2)
	s_add_i32 m0, s38, 0x2800
	v_mad_u32_u16 v142, v76, v249, v144 op_sel:[1,0,0,0]
	global_load_lds_dwordx4 v142, s[10:11]
	s_add_i32 m0, s38, 0x2c00
	v_mad_u32_u16 v143, v80, v249, v145 op_sel:[1,0,0,0]
	global_load_lds_dwordx4 v143, s[10:11]
	v_cvt_scalef32_pk_bf16_fp4 v98, v90, 1.0
	v_cvt_scalef32_pk_bf16_fp4 v99, v90, 1.0 op_sel:[1,0,0]
	v_cvt_scalef32_pk_bf16_fp4 v100, v90, 1.0 op_sel:[0,1,0]
	v_cvt_scalef32_pk_bf16_fp4 v101, v90, 1.0 op_sel:[1,1,0]
	v_cvt_scalef32_pk_bf16_fp4 v102, v91, 1.0
	v_cvt_scalef32_pk_bf16_fp4 v103, v91, 1.0 op_sel:[1,0,0]
	v_cvt_scalef32_pk_bf16_fp4 v104, v91, 1.0 op_sel:[0,1,0]
	v_cvt_scalef32_pk_bf16_fp4 v105, v91, 1.0 op_sel:[1,1,0]
	v_mfma_f32_16x16x32_bf16 v[126:129], v[2:5], v[98:101], 0
	v_cvt_scalef32_pk_bf16_fp4 v98, v92, 1.0
	v_cvt_scalef32_pk_bf16_fp4 v99, v92, 1.0 op_sel:[1,0,0]
	v_cvt_scalef32_pk_bf16_fp4 v100, v92, 1.0 op_sel:[0,1,0]
	v_cvt_scalef32_pk_bf16_fp4 v101, v92, 1.0 op_sel:[1,1,0]
	v_mfma_f32_16x16x32_bf16 v[126:129], v[6:9], v[102:105], v[126:129]
	v_cvt_scalef32_pk_bf16_fp4 v102, v93, 1.0
	v_cvt_scalef32_pk_bf16_fp4 v103, v93, 1.0 op_sel:[1,0,0]
	v_cvt_scalef32_pk_bf16_fp4 v104, v93, 1.0 op_sel:[0,1,0]
	v_cvt_scalef32_pk_bf16_fp4 v105, v93, 1.0 op_sel:[1,1,0]
	v_mfma_f32_16x16x32_bf16 v[126:129], v[10:13], v[98:101], v[126:129]
	v_cvt_scalef32_pk_bf16_fp4 v98, v94, 1.0
	v_cvt_scalef32_pk_bf16_fp4 v99, v94, 1.0 op_sel:[1,0,0]
	v_cvt_scalef32_pk_bf16_fp4 v100, v94, 1.0 op_sel:[0,1,0]
	v_cvt_scalef32_pk_bf16_fp4 v101, v94, 1.0 op_sel:[1,1,0]
	v_mfma_f32_16x16x32_bf16 v[126:129], v[14:17], v[102:105], v[126:129]
	v_cvt_scalef32_pk_bf16_fp4 v102, v95, 1.0
	v_cvt_scalef32_pk_bf16_fp4 v103, v95, 1.0 op_sel:[1,0,0]
	v_cvt_scalef32_pk_bf16_fp4 v104, v95, 1.0 op_sel:[0,1,0]
	v_cvt_scalef32_pk_bf16_fp4 v105, v95, 1.0 op_sel:[1,1,0]
	v_mfma_f32_16x16x32_bf16 v[126:129], v[18:21], v[98:101], v[126:129]
	v_cvt_scalef32_pk_bf16_fp4 v98, v96, 1.0
	v_cvt_scalef32_pk_bf16_fp4 v99, v96, 1.0 op_sel:[1,0,0]
	v_cvt_scalef32_pk_bf16_fp4 v100, v96, 1.0 op_sel:[0,1,0]
	v_cvt_scalef32_pk_bf16_fp4 v101, v96, 1.0 op_sel:[1,1,0]
	v_mfma_f32_16x16x32_bf16 v[126:129], v[22:25], v[102:105], v[126:129]
	v_cvt_scalef32_pk_bf16_fp4 v102, v97, 1.0
	v_cvt_scalef32_pk_bf16_fp4 v103, v97, 1.0 op_sel:[1,0,0]
	v_cvt_scalef32_pk_bf16_fp4 v104, v97, 1.0 op_sel:[0,1,0]
	v_cvt_scalef32_pk_bf16_fp4 v105, v97, 1.0 op_sel:[1,1,0]
	v_mfma_f32_16x16x32_bf16 v[126:129], v[26:29], v[98:101], v[126:129]
	v_cvt_pk_bf16_f32 v139, v114, v118
	v_mfma_f32_16x16x32_bf16 v[126:129], v[30:33], v[102:105], v[126:129]
	s_waitcnt vmcnt(23)
	ds_read_b128 v[90:93], v146 offset:14336
	ds_read_b128 v[94:97], v147 offset:14336
	s_waitcnt lgkmcnt(2)
	s_add_i32 m0, s38, 0x3000
	v_mad_u32_u16 v142, v77, v249, v144
	global_load_lds_dwordx4 v142, s[10:11]
	s_add_i32 m0, s38, 0x3400
	v_mad_u32_u16 v143, v81, v249, v145
	global_load_lds_dwordx4 v143, s[10:11]
	v_cvt_scalef32_pk_bf16_fp4 v98, v82, 1.0
	v_cvt_scalef32_pk_bf16_fp4 v99, v82, 1.0 op_sel:[1,0,0]
	v_cvt_scalef32_pk_bf16_fp4 v100, v82, 1.0 op_sel:[0,1,0]
	v_cvt_scalef32_pk_bf16_fp4 v101, v82, 1.0 op_sel:[1,1,0]
	v_cvt_scalef32_pk_bf16_fp4 v102, v83, 1.0
	v_cvt_scalef32_pk_bf16_fp4 v103, v83, 1.0 op_sel:[1,0,0]
	v_cvt_scalef32_pk_bf16_fp4 v104, v83, 1.0 op_sel:[0,1,0]
	v_cvt_scalef32_pk_bf16_fp4 v105, v83, 1.0 op_sel:[1,1,0]
	v_mfma_f32_16x16x32_bf16 v[130:133], v[2:5], v[98:101], 0
	v_cvt_scalef32_pk_bf16_fp4 v98, v84, 1.0
	v_cvt_scalef32_pk_bf16_fp4 v99, v84, 1.0 op_sel:[1,0,0]
	v_cvt_scalef32_pk_bf16_fp4 v100, v84, 1.0 op_sel:[0,1,0]
	v_cvt_scalef32_pk_bf16_fp4 v101, v84, 1.0 op_sel:[1,1,0]
	v_mfma_f32_16x16x32_bf16 v[130:133], v[6:9], v[102:105], v[130:133]
	v_cvt_scalef32_pk_bf16_fp4 v102, v85, 1.0
	v_cvt_scalef32_pk_bf16_fp4 v103, v85, 1.0 op_sel:[1,0,0]
	v_cvt_scalef32_pk_bf16_fp4 v104, v85, 1.0 op_sel:[0,1,0]
	v_cvt_scalef32_pk_bf16_fp4 v105, v85, 1.0 op_sel:[1,1,0]
	v_mfma_f32_16x16x32_bf16 v[130:133], v[10:13], v[98:101], v[130:133]
	v_cvt_scalef32_pk_bf16_fp4 v98, v86, 1.0
	v_cvt_scalef32_pk_bf16_fp4 v99, v86, 1.0 op_sel:[1,0,0]
	v_cvt_scalef32_pk_bf16_fp4 v100, v86, 1.0 op_sel:[0,1,0]
	v_cvt_scalef32_pk_bf16_fp4 v101, v86, 1.0 op_sel:[1,1,0]
	v_mfma_f32_16x16x32_bf16 v[130:133], v[14:17], v[102:105], v[130:133]
	v_cvt_scalef32_pk_bf16_fp4 v102, v87, 1.0
	v_cvt_scalef32_pk_bf16_fp4 v103, v87, 1.0 op_sel:[1,0,0]
	v_cvt_scalef32_pk_bf16_fp4 v104, v87, 1.0 op_sel:[0,1,0]
	v_cvt_scalef32_pk_bf16_fp4 v105, v87, 1.0 op_sel:[1,1,0]
	v_mfma_f32_16x16x32_bf16 v[130:133], v[18:21], v[98:101], v[130:133]
	v_cvt_scalef32_pk_bf16_fp4 v98, v88, 1.0
	v_cvt_scalef32_pk_bf16_fp4 v99, v88, 1.0 op_sel:[1,0,0]
	v_cvt_scalef32_pk_bf16_fp4 v100, v88, 1.0 op_sel:[0,1,0]
	v_cvt_scalef32_pk_bf16_fp4 v101, v88, 1.0 op_sel:[1,1,0]
	v_mfma_f32_16x16x32_bf16 v[130:133], v[22:25], v[102:105], v[130:133]
	v_cvt_scalef32_pk_bf16_fp4 v102, v89, 1.0
	v_cvt_scalef32_pk_bf16_fp4 v103, v89, 1.0 op_sel:[1,0,0]
	v_cvt_scalef32_pk_bf16_fp4 v104, v89, 1.0 op_sel:[0,1,0]
	v_cvt_scalef32_pk_bf16_fp4 v105, v89, 1.0 op_sel:[1,1,0]
	v_mfma_f32_16x16x32_bf16 v[130:133], v[26:29], v[98:101], v[130:133]
	v_mfma_f32_16x16x32_bf16 v[130:133], v[30:33], v[102:105], v[130:133]
	s_waitcnt vmcnt(12)
	ds_read_b128 v[82:85], v146
	ds_read_b128 v[86:89], v147
	s_waitcnt lgkmcnt(2)
	s_add_i32 m0, s38, 0x3800
	v_mad_u32_u16 v142, v77, v249, v144 op_sel:[1,0,0,0]
	global_load_lds_dwordx4 v142, s[10:11]
	s_add_i32 m0, s38, 0x3c00
	v_mad_u32_u16 v143, v81, v249, v145 op_sel:[1,0,0,0]
	global_load_lds_dwordx4 v143, s[10:11]
	v_cvt_scalef32_pk_bf16_fp4 v98, v90, 1.0
	v_cvt_scalef32_pk_bf16_fp4 v99, v90, 1.0 op_sel:[1,0,0]
	v_cvt_scalef32_pk_bf16_fp4 v100, v90, 1.0 op_sel:[0,1,0]
	v_cvt_scalef32_pk_bf16_fp4 v101, v90, 1.0 op_sel:[1,1,0]
	v_cvt_scalef32_pk_bf16_fp4 v102, v91, 1.0
	v_cvt_scalef32_pk_bf16_fp4 v103, v91, 1.0 op_sel:[1,0,0]
	v_cvt_scalef32_pk_bf16_fp4 v104, v91, 1.0 op_sel:[0,1,0]
	v_cvt_scalef32_pk_bf16_fp4 v105, v91, 1.0 op_sel:[1,1,0]
	v_mfma_f32_16x16x32_bf16 v[134:137], v[2:5], v[98:101], 0
	v_cvt_scalef32_pk_bf16_fp4 v98, v92, 1.0
	v_cvt_scalef32_pk_bf16_fp4 v99, v92, 1.0 op_sel:[1,0,0]
	v_cvt_scalef32_pk_bf16_fp4 v100, v92, 1.0 op_sel:[0,1,0]
	v_cvt_scalef32_pk_bf16_fp4 v101, v92, 1.0 op_sel:[1,1,0]
	v_mfma_f32_16x16x32_bf16 v[134:137], v[6:9], v[102:105], v[134:137]
	v_cvt_scalef32_pk_bf16_fp4 v102, v93, 1.0
	v_cvt_scalef32_pk_bf16_fp4 v103, v93, 1.0 op_sel:[1,0,0]
	v_cvt_scalef32_pk_bf16_fp4 v104, v93, 1.0 op_sel:[0,1,0]
	v_cvt_scalef32_pk_bf16_fp4 v105, v93, 1.0 op_sel:[1,1,0]
	v_mfma_f32_16x16x32_bf16 v[134:137], v[10:13], v[98:101], v[134:137]
	v_cvt_scalef32_pk_bf16_fp4 v98, v94, 1.0
	v_cvt_scalef32_pk_bf16_fp4 v99, v94, 1.0 op_sel:[1,0,0]
	v_cvt_scalef32_pk_bf16_fp4 v100, v94, 1.0 op_sel:[0,1,0]
	v_cvt_scalef32_pk_bf16_fp4 v101, v94, 1.0 op_sel:[1,1,0]
	v_mfma_f32_16x16x32_bf16 v[134:137], v[14:17], v[102:105], v[134:137]
	v_cvt_scalef32_pk_bf16_fp4 v102, v95, 1.0
	v_cvt_scalef32_pk_bf16_fp4 v103, v95, 1.0 op_sel:[1,0,0]
	v_cvt_scalef32_pk_bf16_fp4 v104, v95, 1.0 op_sel:[0,1,0]
	v_cvt_scalef32_pk_bf16_fp4 v105, v95, 1.0 op_sel:[1,1,0]
	v_mfma_f32_16x16x32_bf16 v[134:137], v[18:21], v[98:101], v[134:137]
	v_cvt_scalef32_pk_bf16_fp4 v98, v96, 1.0
	v_cvt_scalef32_pk_bf16_fp4 v99, v96, 1.0 op_sel:[1,0,0]
	v_cvt_scalef32_pk_bf16_fp4 v100, v96, 1.0 op_sel:[0,1,0]
	v_cvt_scalef32_pk_bf16_fp4 v101, v96, 1.0 op_sel:[1,1,0]
	v_mfma_f32_16x16x32_bf16 v[134:137], v[22:25], v[102:105], v[134:137]
	v_cvt_scalef32_pk_bf16_fp4 v102, v97, 1.0
	v_cvt_scalef32_pk_bf16_fp4 v103, v97, 1.0 op_sel:[1,0,0]
	v_cvt_scalef32_pk_bf16_fp4 v104, v97, 1.0 op_sel:[0,1,0]
	v_cvt_scalef32_pk_bf16_fp4 v105, v97, 1.0 op_sel:[1,1,0]
	v_mfma_f32_16x16x32_bf16 v[134:137], v[26:29], v[98:101], v[134:137]
	v_cvt_pk_bf16_f32 v140, v122, v126
	v_mfma_f32_16x16x32_bf16 v[134:137], v[30:33], v[102:105], v[134:137]
	s_nop 7
	s_nop 7
	v_cvt_pk_bf16_f32 v141, v130, v134
	s_mov_b64 exec, 0xffff
	global_store_dwordx4 v151, v[138:141], s[4:5]
	s_mov_b64 exec, -1
	v_add_u32_e32 v151, 0x100, v151
	global_load_dwordx4 v[2:5], v150, s[2:3]
	global_load_dwordx4 v[6:9], v150, s[2:3] offset:16
	global_load_dwordx4 v[10:13], v150, s[2:3] offset:32
	global_load_dwordx4 v[14:17], v150, s[2:3] offset:48
	global_load_dwordx4 v[18:21], v150, s[2:3] offset:256
	global_load_dwordx4 v[22:25], v150, s[2:3] offset:272
	global_load_dwordx4 v[26:29], v150, s[2:3] offset:288
	global_load_dwordx4 v[30:33], v150, s[2:3] offset:304
	v_add_u32_e32 v150, 0x1000, v150
	global_load_dwordx4 v[74:77], v149, s[22:23]
	global_load_dwordx4 v[78:81], v149, s[22:23] offset:16
	v_add_u32_e32 v149, s41, v149
	s_waitcnt vmcnt(23)
	ds_read_b128 v[90:93], v146 offset:2048
	ds_read_b128 v[94:97], v147 offset:2048
	s_waitcnt lgkmcnt(2)
	s_add_i32 m0, s38, 0x0
	v_mad_u32_u16 v142, v66, v249, v144
	global_load_lds_dwordx4 v142, s[10:11]
	s_add_i32 m0, s38, 0x400
	v_mad_u32_u16 v143, v70, v249, v145
	global_load_lds_dwordx4 v143, s[10:11]
	v_cvt_scalef32_pk_bf16_fp4 v98, v82, 1.0
	v_cvt_scalef32_pk_bf16_fp4 v99, v82, 1.0 op_sel:[1,0,0]
	v_cvt_scalef32_pk_bf16_fp4 v100, v82, 1.0 op_sel:[0,1,0]
	v_cvt_scalef32_pk_bf16_fp4 v101, v82, 1.0 op_sel:[1,1,0]
	v_cvt_scalef32_pk_bf16_fp4 v102, v83, 1.0
	v_cvt_scalef32_pk_bf16_fp4 v103, v83, 1.0 op_sel:[1,0,0]
	v_cvt_scalef32_pk_bf16_fp4 v104, v83, 1.0 op_sel:[0,1,0]
	v_cvt_scalef32_pk_bf16_fp4 v105, v83, 1.0 op_sel:[1,1,0]
	v_mfma_f32_16x16x32_bf16 v[106:109], v[34:37], v[98:101], 0
	v_cvt_scalef32_pk_bf16_fp4 v98, v84, 1.0
	v_cvt_scalef32_pk_bf16_fp4 v99, v84, 1.0 op_sel:[1,0,0]
	v_cvt_scalef32_pk_bf16_fp4 v100, v84, 1.0 op_sel:[0,1,0]
	v_cvt_scalef32_pk_bf16_fp4 v101, v84, 1.0 op_sel:[1,1,0]
	v_mfma_f32_16x16x32_bf16 v[106:109], v[38:41], v[102:105], v[106:109]
	v_cvt_scalef32_pk_bf16_fp4 v102, v85, 1.0
	v_cvt_scalef32_pk_bf16_fp4 v103, v85, 1.0 op_sel:[1,0,0]
	v_cvt_scalef32_pk_bf16_fp4 v104, v85, 1.0 op_sel:[0,1,0]
	v_cvt_scalef32_pk_bf16_fp4 v105, v85, 1.0 op_sel:[1,1,0]
	v_mfma_f32_16x16x32_bf16 v[106:109], v[42:45], v[98:101], v[106:109]
	v_cvt_scalef32_pk_bf16_fp4 v98, v86, 1.0
	v_cvt_scalef32_pk_bf16_fp4 v99, v86, 1.0 op_sel:[1,0,0]
	v_cvt_scalef32_pk_bf16_fp4 v100, v86, 1.0 op_sel:[0,1,0]
	v_cvt_scalef32_pk_bf16_fp4 v101, v86, 1.0 op_sel:[1,1,0]
	v_mfma_f32_16x16x32_bf16 v[106:109], v[46:49], v[102:105], v[106:109]
	v_cvt_scalef32_pk_bf16_fp4 v102, v87, 1.0
	v_cvt_scalef32_pk_bf16_fp4 v103, v87, 1.0 op_sel:[1,0,0]
	v_cvt_scalef32_pk_bf16_fp4 v104, v87, 1.0 op_sel:[0,1,0]
	v_cvt_scalef32_pk_bf16_fp4 v105, v87, 1.0 op_sel:[1,1,0]
	v_mfma_f32_16x16x32_bf16 v[106:109], v[50:53], v[98:101], v[106:109]
	v_cvt_scalef32_pk_bf16_fp4 v98, v88, 1.0
	v_cvt_scalef32_pk_bf16_fp4 v99, v88, 1.0 op_sel:[1,0,0]
	v_cvt_scalef32_pk_bf16_fp4 v100, v88, 1.0 op_sel:[0,1,0]
	v_cvt_scalef32_pk_bf16_fp4 v101, v88, 1.0 op_sel:[1,1,0]
	v_mfma_f32_16x16x32_bf16 v[106:109], v[54:57], v[102:105], v[106:109]
	v_cvt_scalef32_pk_bf16_fp4 v102, v89, 1.0
	v_cvt_scalef32_pk_bf16_fp4 v103, v89, 1.0 op_sel:[1,0,0]
	v_cvt_scalef32_pk_bf16_fp4 v104, v89, 1.0 op_sel:[0,1,0]
	v_cvt_scalef32_pk_bf16_fp4 v105, v89, 1.0 op_sel:[1,1,0]
	v_mfma_f32_16x16x32_bf16 v[106:109], v[58:61], v[98:101], v[106:109]
	v_mfma_f32_16x16x32_bf16 v[106:109], v[62:65], v[102:105], v[106:109]
	s_waitcnt vmcnt(23)
	ds_read_b128 v[82:85], v146 offset:4096
	ds_read_b128 v[86:89], v147 offset:4096
	s_waitcnt lgkmcnt(2)
	s_add_i32 m0, s38, 0x800
	v_mad_u32_u16 v142, v66, v249, v144 op_sel:[1,0,0,0]
	global_load_lds_dwordx4 v142, s[10:11]
	s_add_i32 m0, s38, 0xc00
	v_mad_u32_u16 v143, v70, v249, v145 op_sel:[1,0,0,0]
	global_load_lds_dwordx4 v143, s[10:11]
	v_cvt_scalef32_pk_bf16_fp4 v98, v90, 1.0
	v_cvt_scalef32_pk_bf16_fp4 v99, v90, 1.0 op_sel:[1,0,0]
	v_cvt_scalef32_pk_bf16_fp4 v100, v90, 1.0 op_sel:[0,1,0]
	v_cvt_scalef32_pk_bf16_fp4 v101, v90, 1.0 op_sel:[1,1,0]
	v_cvt_scalef32_pk_bf16_fp4 v102, v91, 1.0
	v_cvt_scalef32_pk_bf16_fp4 v103, v91, 1.0 op_sel:[1,0,0]
	v_cvt_scalef32_pk_bf16_fp4 v104, v91, 1.0 op_sel:[0,1,0]
	v_cvt_scalef32_pk_bf16_fp4 v105, v91, 1.0 op_sel:[1,1,0]
	v_mfma_f32_16x16x32_bf16 v[110:113], v[34:37], v[98:101], 0
	v_cvt_scalef32_pk_bf16_fp4 v98, v92, 1.0
	v_cvt_scalef32_pk_bf16_fp4 v99, v92, 1.0 op_sel:[1,0,0]
	v_cvt_scalef32_pk_bf16_fp4 v100, v92, 1.0 op_sel:[0,1,0]
	v_cvt_scalef32_pk_bf16_fp4 v101, v92, 1.0 op_sel:[1,1,0]
	v_mfma_f32_16x16x32_bf16 v[110:113], v[38:41], v[102:105], v[110:113]
	v_cvt_scalef32_pk_bf16_fp4 v102, v93, 1.0
	v_cvt_scalef32_pk_bf16_fp4 v103, v93, 1.0 op_sel:[1,0,0]
	v_cvt_scalef32_pk_bf16_fp4 v104, v93, 1.0 op_sel:[0,1,0]
	v_cvt_scalef32_pk_bf16_fp4 v105, v93, 1.0 op_sel:[1,1,0]
	v_mfma_f32_16x16x32_bf16 v[110:113], v[42:45], v[98:101], v[110:113]
	v_cvt_scalef32_pk_bf16_fp4 v98, v94, 1.0
	v_cvt_scalef32_pk_bf16_fp4 v99, v94, 1.0 op_sel:[1,0,0]
	v_cvt_scalef32_pk_bf16_fp4 v100, v94, 1.0 op_sel:[0,1,0]
	v_cvt_scalef32_pk_bf16_fp4 v101, v94, 1.0 op_sel:[1,1,0]
	v_mfma_f32_16x16x32_bf16 v[110:113], v[46:49], v[102:105], v[110:113]
	v_cvt_scalef32_pk_bf16_fp4 v102, v95, 1.0
	v_cvt_scalef32_pk_bf16_fp4 v103, v95, 1.0 op_sel:[1,0,0]
	v_cvt_scalef32_pk_bf16_fp4 v104, v95, 1.0 op_sel:[0,1,0]
	v_cvt_scalef32_pk_bf16_fp4 v105, v95, 1.0 op_sel:[1,1,0]
	v_mfma_f32_16x16x32_bf16 v[110:113], v[50:53], v[98:101], v[110:113]
	v_cvt_scalef32_pk_bf16_fp4 v98, v96, 1.0
	v_cvt_scalef32_pk_bf16_fp4 v99, v96, 1.0 op_sel:[1,0,0]
	v_cvt_scalef32_pk_bf16_fp4 v100, v96, 1.0 op_sel:[0,1,0]
	v_cvt_scalef32_pk_bf16_fp4 v101, v96, 1.0 op_sel:[1,1,0]
	v_mfma_f32_16x16x32_bf16 v[110:113], v[54:57], v[102:105], v[110:113]
	v_cvt_scalef32_pk_bf16_fp4 v102, v97, 1.0
	v_cvt_scalef32_pk_bf16_fp4 v103, v97, 1.0 op_sel:[1,0,0]
	v_cvt_scalef32_pk_bf16_fp4 v104, v97, 1.0 op_sel:[0,1,0]
	v_cvt_scalef32_pk_bf16_fp4 v105, v97, 1.0 op_sel:[1,1,0]
	v_mfma_f32_16x16x32_bf16 v[110:113], v[58:61], v[98:101], v[110:113]
	v_mfma_f32_16x16x32_bf16 v[110:113], v[62:65], v[102:105], v[110:113]
	s_waitcnt vmcnt(23)
	ds_read_b128 v[90:93], v146 offset:6144
	ds_read_b128 v[94:97], v147 offset:6144
	s_waitcnt lgkmcnt(2)
	s_add_i32 m0, s38, 0x1000
	v_mad_u32_u16 v142, v67, v249, v144
	global_load_lds_dwordx4 v142, s[10:11]
	s_add_i32 m0, s38, 0x1400
	v_mad_u32_u16 v143, v71, v249, v145
	global_load_lds_dwordx4 v143, s[10:11]
	v_cvt_scalef32_pk_bf16_fp4 v98, v82, 1.0
	v_cvt_scalef32_pk_bf16_fp4 v99, v82, 1.0 op_sel:[1,0,0]
	v_cvt_scalef32_pk_bf16_fp4 v100, v82, 1.0 op_sel:[0,1,0]
	v_cvt_scalef32_pk_bf16_fp4 v101, v82, 1.0 op_sel:[1,1,0]
	v_cvt_scalef32_pk_bf16_fp4 v102, v83, 1.0
	v_cvt_scalef32_pk_bf16_fp4 v103, v83, 1.0 op_sel:[1,0,0]
	v_cvt_scalef32_pk_bf16_fp4 v104, v83, 1.0 op_sel:[0,1,0]
	v_cvt_scalef32_pk_bf16_fp4 v105, v83, 1.0 op_sel:[1,1,0]
	v_mfma_f32_16x16x32_bf16 v[114:117], v[34:37], v[98:101], 0
	v_cvt_scalef32_pk_bf16_fp4 v98, v84, 1.0
	v_cvt_scalef32_pk_bf16_fp4 v99, v84, 1.0 op_sel:[1,0,0]
	v_cvt_scalef32_pk_bf16_fp4 v100, v84, 1.0 op_sel:[0,1,0]
	v_cvt_scalef32_pk_bf16_fp4 v101, v84, 1.0 op_sel:[1,1,0]
	v_mfma_f32_16x16x32_bf16 v[114:117], v[38:41], v[102:105], v[114:117]
	v_cvt_scalef32_pk_bf16_fp4 v102, v85, 1.0
	v_cvt_scalef32_pk_bf16_fp4 v103, v85, 1.0 op_sel:[1,0,0]
	v_cvt_scalef32_pk_bf16_fp4 v104, v85, 1.0 op_sel:[0,1,0]
	v_cvt_scalef32_pk_bf16_fp4 v105, v85, 1.0 op_sel:[1,1,0]
	v_mfma_f32_16x16x32_bf16 v[114:117], v[42:45], v[98:101], v[114:117]
	v_cvt_scalef32_pk_bf16_fp4 v98, v86, 1.0
	v_cvt_scalef32_pk_bf16_fp4 v99, v86, 1.0 op_sel:[1,0,0]
	v_cvt_scalef32_pk_bf16_fp4 v100, v86, 1.0 op_sel:[0,1,0]
	v_cvt_scalef32_pk_bf16_fp4 v101, v86, 1.0 op_sel:[1,1,0]
	v_mfma_f32_16x16x32_bf16 v[114:117], v[46:49], v[102:105], v[114:117]
	v_cvt_scalef32_pk_bf16_fp4 v102, v87, 1.0
	v_cvt_scalef32_pk_bf16_fp4 v103, v87, 1.0 op_sel:[1,0,0]
	v_cvt_scalef32_pk_bf16_fp4 v104, v87, 1.0 op_sel:[0,1,0]
	v_cvt_scalef32_pk_bf16_fp4 v105, v87, 1.0 op_sel:[1,1,0]
	v_mfma_f32_16x16x32_bf16 v[114:117], v[50:53], v[98:101], v[114:117]
	v_cvt_scalef32_pk_bf16_fp4 v98, v88, 1.0
	v_cvt_scalef32_pk_bf16_fp4 v99, v88, 1.0 op_sel:[1,0,0]
	v_cvt_scalef32_pk_bf16_fp4 v100, v88, 1.0 op_sel:[0,1,0]
	v_cvt_scalef32_pk_bf16_fp4 v101, v88, 1.0 op_sel:[1,1,0]
	v_mfma_f32_16x16x32_bf16 v[114:117], v[54:57], v[102:105], v[114:117]
	v_cvt_scalef32_pk_bf16_fp4 v102, v89, 1.0
	v_cvt_scalef32_pk_bf16_fp4 v103, v89, 1.0 op_sel:[1,0,0]
	v_cvt_scalef32_pk_bf16_fp4 v104, v89, 1.0 op_sel:[0,1,0]
	v_cvt_scalef32_pk_bf16_fp4 v105, v89, 1.0 op_sel:[1,1,0]
	v_mfma_f32_16x16x32_bf16 v[114:117], v[58:61], v[98:101], v[114:117]
	v_mfma_f32_16x16x32_bf16 v[114:117], v[62:65], v[102:105], v[114:117]
	s_waitcnt vmcnt(23)
	ds_read_b128 v[82:85], v146 offset:8192
	ds_read_b128 v[86:89], v147 offset:8192
	s_waitcnt lgkmcnt(2)
	s_add_i32 m0, s38, 0x1800
	v_mad_u32_u16 v142, v67, v249, v144 op_sel:[1,0,0,0]
	global_load_lds_dwordx4 v142, s[10:11]
	s_add_i32 m0, s38, 0x1c00
	v_mad_u32_u16 v143, v71, v249, v145 op_sel:[1,0,0,0]
	global_load_lds_dwordx4 v143, s[10:11]
	v_cvt_scalef32_pk_bf16_fp4 v98, v90, 1.0
	v_cvt_scalef32_pk_bf16_fp4 v99, v90, 1.0 op_sel:[1,0,0]
	v_cvt_scalef32_pk_bf16_fp4 v100, v90, 1.0 op_sel:[0,1,0]
	v_cvt_scalef32_pk_bf16_fp4 v101, v90, 1.0 op_sel:[1,1,0]
	v_cvt_scalef32_pk_bf16_fp4 v102, v91, 1.0
	v_cvt_scalef32_pk_bf16_fp4 v103, v91, 1.0 op_sel:[1,0,0]
	v_cvt_scalef32_pk_bf16_fp4 v104, v91, 1.0 op_sel:[0,1,0]
	v_cvt_scalef32_pk_bf16_fp4 v105, v91, 1.0 op_sel:[1,1,0]
	v_mfma_f32_16x16x32_bf16 v[118:121], v[34:37], v[98:101], 0
	v_cvt_scalef32_pk_bf16_fp4 v98, v92, 1.0
	v_cvt_scalef32_pk_bf16_fp4 v99, v92, 1.0 op_sel:[1,0,0]
	v_cvt_scalef32_pk_bf16_fp4 v100, v92, 1.0 op_sel:[0,1,0]
	v_cvt_scalef32_pk_bf16_fp4 v101, v92, 1.0 op_sel:[1,1,0]
	v_mfma_f32_16x16x32_bf16 v[118:121], v[38:41], v[102:105], v[118:121]
	v_cvt_scalef32_pk_bf16_fp4 v102, v93, 1.0
	v_cvt_scalef32_pk_bf16_fp4 v103, v93, 1.0 op_sel:[1,0,0]
	v_cvt_scalef32_pk_bf16_fp4 v104, v93, 1.0 op_sel:[0,1,0]
	v_cvt_scalef32_pk_bf16_fp4 v105, v93, 1.0 op_sel:[1,1,0]
	v_mfma_f32_16x16x32_bf16 v[118:121], v[42:45], v[98:101], v[118:121]
	v_cvt_scalef32_pk_bf16_fp4 v98, v94, 1.0
	v_cvt_scalef32_pk_bf16_fp4 v99, v94, 1.0 op_sel:[1,0,0]
	v_cvt_scalef32_pk_bf16_fp4 v100, v94, 1.0 op_sel:[0,1,0]
	v_cvt_scalef32_pk_bf16_fp4 v101, v94, 1.0 op_sel:[1,1,0]
	v_mfma_f32_16x16x32_bf16 v[118:121], v[46:49], v[102:105], v[118:121]
	v_cvt_scalef32_pk_bf16_fp4 v102, v95, 1.0
	v_cvt_scalef32_pk_bf16_fp4 v103, v95, 1.0 op_sel:[1,0,0]
	v_cvt_scalef32_pk_bf16_fp4 v104, v95, 1.0 op_sel:[0,1,0]
	v_cvt_scalef32_pk_bf16_fp4 v105, v95, 1.0 op_sel:[1,1,0]
	v_mfma_f32_16x16x32_bf16 v[118:121], v[50:53], v[98:101], v[118:121]
	v_cvt_scalef32_pk_bf16_fp4 v98, v96, 1.0
	v_cvt_scalef32_pk_bf16_fp4 v99, v96, 1.0 op_sel:[1,0,0]
	v_cvt_scalef32_pk_bf16_fp4 v100, v96, 1.0 op_sel:[0,1,0]
	v_cvt_scalef32_pk_bf16_fp4 v101, v96, 1.0 op_sel:[1,1,0]
	v_mfma_f32_16x16x32_bf16 v[118:121], v[54:57], v[102:105], v[118:121]
	v_cvt_scalef32_pk_bf16_fp4 v102, v97, 1.0
	v_cvt_scalef32_pk_bf16_fp4 v103, v97, 1.0 op_sel:[1,0,0]
	v_cvt_scalef32_pk_bf16_fp4 v104, v97, 1.0 op_sel:[0,1,0]
	v_cvt_scalef32_pk_bf16_fp4 v105, v97, 1.0 op_sel:[1,1,0]
	v_mfma_f32_16x16x32_bf16 v[118:121], v[58:61], v[98:101], v[118:121]
	v_cvt_pk_bf16_f32 v138, v106, v110
	v_mfma_f32_16x16x32_bf16 v[118:121], v[62:65], v[102:105], v[118:121]
	s_waitcnt vmcnt(23)
	ds_read_b128 v[90:93], v146 offset:10240
	ds_read_b128 v[94:97], v147 offset:10240
	s_waitcnt lgkmcnt(2)
	s_add_i32 m0, s38, 0x2000
	v_mad_u32_u16 v142, v68, v249, v144
	global_load_lds_dwordx4 v142, s[10:11]
	s_add_i32 m0, s38, 0x2400
	v_mad_u32_u16 v143, v72, v249, v145
	global_load_lds_dwordx4 v143, s[10:11]
	v_cvt_scalef32_pk_bf16_fp4 v98, v82, 1.0
	v_cvt_scalef32_pk_bf16_fp4 v99, v82, 1.0 op_sel:[1,0,0]
	v_cvt_scalef32_pk_bf16_fp4 v100, v82, 1.0 op_sel:[0,1,0]
	v_cvt_scalef32_pk_bf16_fp4 v101, v82, 1.0 op_sel:[1,1,0]
	v_cvt_scalef32_pk_bf16_fp4 v102, v83, 1.0
	v_cvt_scalef32_pk_bf16_fp4 v103, v83, 1.0 op_sel:[1,0,0]
	v_cvt_scalef32_pk_bf16_fp4 v104, v83, 1.0 op_sel:[0,1,0]
	v_cvt_scalef32_pk_bf16_fp4 v105, v83, 1.0 op_sel:[1,1,0]
	v_mfma_f32_16x16x32_bf16 v[122:125], v[34:37], v[98:101], 0
	v_cvt_scalef32_pk_bf16_fp4 v98, v84, 1.0
	v_cvt_scalef32_pk_bf16_fp4 v99, v84, 1.0 op_sel:[1,0,0]
	v_cvt_scalef32_pk_bf16_fp4 v100, v84, 1.0 op_sel:[0,1,0]
	v_cvt_scalef32_pk_bf16_fp4 v101, v84, 1.0 op_sel:[1,1,0]
	v_mfma_f32_16x16x32_bf16 v[122:125], v[38:41], v[102:105], v[122:125]
	v_cvt_scalef32_pk_bf16_fp4 v102, v85, 1.0
	v_cvt_scalef32_pk_bf16_fp4 v103, v85, 1.0 op_sel:[1,0,0]
	v_cvt_scalef32_pk_bf16_fp4 v104, v85, 1.0 op_sel:[0,1,0]
	v_cvt_scalef32_pk_bf16_fp4 v105, v85, 1.0 op_sel:[1,1,0]
	v_mfma_f32_16x16x32_bf16 v[122:125], v[42:45], v[98:101], v[122:125]
	v_cvt_scalef32_pk_bf16_fp4 v98, v86, 1.0
	v_cvt_scalef32_pk_bf16_fp4 v99, v86, 1.0 op_sel:[1,0,0]
	v_cvt_scalef32_pk_bf16_fp4 v100, v86, 1.0 op_sel:[0,1,0]
	v_cvt_scalef32_pk_bf16_fp4 v101, v86, 1.0 op_sel:[1,1,0]
	v_mfma_f32_16x16x32_bf16 v[122:125], v[46:49], v[102:105], v[122:125]
	v_cvt_scalef32_pk_bf16_fp4 v102, v87, 1.0
	v_cvt_scalef32_pk_bf16_fp4 v103, v87, 1.0 op_sel:[1,0,0]
	v_cvt_scalef32_pk_bf16_fp4 v104, v87, 1.0 op_sel:[0,1,0]
	v_cvt_scalef32_pk_bf16_fp4 v105, v87, 1.0 op_sel:[1,1,0]
	v_mfma_f32_16x16x32_bf16 v[122:125], v[50:53], v[98:101], v[122:125]
	v_cvt_scalef32_pk_bf16_fp4 v98, v88, 1.0
	v_cvt_scalef32_pk_bf16_fp4 v99, v88, 1.0 op_sel:[1,0,0]
	v_cvt_scalef32_pk_bf16_fp4 v100, v88, 1.0 op_sel:[0,1,0]
	v_cvt_scalef32_pk_bf16_fp4 v101, v88, 1.0 op_sel:[1,1,0]
	v_mfma_f32_16x16x32_bf16 v[122:125], v[54:57], v[102:105], v[122:125]
	v_cvt_scalef32_pk_bf16_fp4 v102, v89, 1.0
	v_cvt_scalef32_pk_bf16_fp4 v103, v89, 1.0 op_sel:[1,0,0]
	v_cvt_scalef32_pk_bf16_fp4 v104, v89, 1.0 op_sel:[0,1,0]
	v_cvt_scalef32_pk_bf16_fp4 v105, v89, 1.0 op_sel:[1,1,0]
	v_mfma_f32_16x16x32_bf16 v[122:125], v[58:61], v[98:101], v[122:125]
	v_mfma_f32_16x16x32_bf16 v[122:125], v[62:65], v[102:105], v[122:125]
	s_waitcnt vmcnt(23)
	ds_read_b128 v[82:85], v146 offset:12288
	ds_read_b128 v[86:89], v147 offset:12288
	s_waitcnt lgkmcnt(2)
	s_add_i32 m0, s38, 0x2800
	v_mad_u32_u16 v142, v68, v249, v144 op_sel:[1,0,0,0]
	global_load_lds_dwordx4 v142, s[10:11]
	s_add_i32 m0, s38, 0x2c00
	v_mad_u32_u16 v143, v72, v249, v145 op_sel:[1,0,0,0]
	global_load_lds_dwordx4 v143, s[10:11]
	v_cvt_scalef32_pk_bf16_fp4 v98, v90, 1.0
	v_cvt_scalef32_pk_bf16_fp4 v99, v90, 1.0 op_sel:[1,0,0]
	v_cvt_scalef32_pk_bf16_fp4 v100, v90, 1.0 op_sel:[0,1,0]
	v_cvt_scalef32_pk_bf16_fp4 v101, v90, 1.0 op_sel:[1,1,0]
	v_cvt_scalef32_pk_bf16_fp4 v102, v91, 1.0
	v_cvt_scalef32_pk_bf16_fp4 v103, v91, 1.0 op_sel:[1,0,0]
	v_cvt_scalef32_pk_bf16_fp4 v104, v91, 1.0 op_sel:[0,1,0]
	v_cvt_scalef32_pk_bf16_fp4 v105, v91, 1.0 op_sel:[1,1,0]
	v_mfma_f32_16x16x32_bf16 v[126:129], v[34:37], v[98:101], 0
	v_cvt_scalef32_pk_bf16_fp4 v98, v92, 1.0
	v_cvt_scalef32_pk_bf16_fp4 v99, v92, 1.0 op_sel:[1,0,0]
	v_cvt_scalef32_pk_bf16_fp4 v100, v92, 1.0 op_sel:[0,1,0]
	v_cvt_scalef32_pk_bf16_fp4 v101, v92, 1.0 op_sel:[1,1,0]
	v_mfma_f32_16x16x32_bf16 v[126:129], v[38:41], v[102:105], v[126:129]
	v_cvt_scalef32_pk_bf16_fp4 v102, v93, 1.0
	v_cvt_scalef32_pk_bf16_fp4 v103, v93, 1.0 op_sel:[1,0,0]
	v_cvt_scalef32_pk_bf16_fp4 v104, v93, 1.0 op_sel:[0,1,0]
	v_cvt_scalef32_pk_bf16_fp4 v105, v93, 1.0 op_sel:[1,1,0]
	v_mfma_f32_16x16x32_bf16 v[126:129], v[42:45], v[98:101], v[126:129]
	v_cvt_scalef32_pk_bf16_fp4 v98, v94, 1.0
	v_cvt_scalef32_pk_bf16_fp4 v99, v94, 1.0 op_sel:[1,0,0]
	v_cvt_scalef32_pk_bf16_fp4 v100, v94, 1.0 op_sel:[0,1,0]
	v_cvt_scalef32_pk_bf16_fp4 v101, v94, 1.0 op_sel:[1,1,0]
	v_mfma_f32_16x16x32_bf16 v[126:129], v[46:49], v[102:105], v[126:129]
	v_cvt_scalef32_pk_bf16_fp4 v102, v95, 1.0
	v_cvt_scalef32_pk_bf16_fp4 v103, v95, 1.0 op_sel:[1,0,0]
	v_cvt_scalef32_pk_bf16_fp4 v104, v95, 1.0 op_sel:[0,1,0]
	v_cvt_scalef32_pk_bf16_fp4 v105, v95, 1.0 op_sel:[1,1,0]
	v_mfma_f32_16x16x32_bf16 v[126:129], v[50:53], v[98:101], v[126:129]
	v_cvt_scalef32_pk_bf16_fp4 v98, v96, 1.0
	v_cvt_scalef32_pk_bf16_fp4 v99, v96, 1.0 op_sel:[1,0,0]
	v_cvt_scalef32_pk_bf16_fp4 v100, v96, 1.0 op_sel:[0,1,0]
	v_cvt_scalef32_pk_bf16_fp4 v101, v96, 1.0 op_sel:[1,1,0]
	v_mfma_f32_16x16x32_bf16 v[126:129], v[54:57], v[102:105], v[126:129]
	v_cvt_scalef32_pk_bf16_fp4 v102, v97, 1.0
	v_cvt_scalef32_pk_bf16_fp4 v103, v97, 1.0 op_sel:[1,0,0]
	v_cvt_scalef32_pk_bf16_fp4 v104, v97, 1.0 op_sel:[0,1,0]
	v_cvt_scalef32_pk_bf16_fp4 v105, v97, 1.0 op_sel:[1,1,0]
	v_mfma_f32_16x16x32_bf16 v[126:129], v[58:61], v[98:101], v[126:129]
	v_cvt_pk_bf16_f32 v139, v114, v118
	v_mfma_f32_16x16x32_bf16 v[126:129], v[62:65], v[102:105], v[126:129]
	s_waitcnt vmcnt(23)
	ds_read_b128 v[90:93], v146 offset:14336
	ds_read_b128 v[94:97], v147 offset:14336
	s_waitcnt lgkmcnt(2)
	s_add_i32 m0, s38, 0x3000
	v_mad_u32_u16 v142, v69, v249, v144
	global_load_lds_dwordx4 v142, s[10:11]
	s_add_i32 m0, s38, 0x3400
	v_mad_u32_u16 v143, v73, v249, v145
	global_load_lds_dwordx4 v143, s[10:11]
	v_cvt_scalef32_pk_bf16_fp4 v98, v82, 1.0
	v_cvt_scalef32_pk_bf16_fp4 v99, v82, 1.0 op_sel:[1,0,0]
	v_cvt_scalef32_pk_bf16_fp4 v100, v82, 1.0 op_sel:[0,1,0]
	v_cvt_scalef32_pk_bf16_fp4 v101, v82, 1.0 op_sel:[1,1,0]
	v_cvt_scalef32_pk_bf16_fp4 v102, v83, 1.0
	v_cvt_scalef32_pk_bf16_fp4 v103, v83, 1.0 op_sel:[1,0,0]
	v_cvt_scalef32_pk_bf16_fp4 v104, v83, 1.0 op_sel:[0,1,0]
	v_cvt_scalef32_pk_bf16_fp4 v105, v83, 1.0 op_sel:[1,1,0]
	v_mfma_f32_16x16x32_bf16 v[130:133], v[34:37], v[98:101], 0
	v_cvt_scalef32_pk_bf16_fp4 v98, v84, 1.0
	v_cvt_scalef32_pk_bf16_fp4 v99, v84, 1.0 op_sel:[1,0,0]
	v_cvt_scalef32_pk_bf16_fp4 v100, v84, 1.0 op_sel:[0,1,0]
	v_cvt_scalef32_pk_bf16_fp4 v101, v84, 1.0 op_sel:[1,1,0]
	v_mfma_f32_16x16x32_bf16 v[130:133], v[38:41], v[102:105], v[130:133]
	v_cvt_scalef32_pk_bf16_fp4 v102, v85, 1.0
	v_cvt_scalef32_pk_bf16_fp4 v103, v85, 1.0 op_sel:[1,0,0]
	v_cvt_scalef32_pk_bf16_fp4 v104, v85, 1.0 op_sel:[0,1,0]
	v_cvt_scalef32_pk_bf16_fp4 v105, v85, 1.0 op_sel:[1,1,0]
	v_mfma_f32_16x16x32_bf16 v[130:133], v[42:45], v[98:101], v[130:133]
	v_cvt_scalef32_pk_bf16_fp4 v98, v86, 1.0
	v_cvt_scalef32_pk_bf16_fp4 v99, v86, 1.0 op_sel:[1,0,0]
	v_cvt_scalef32_pk_bf16_fp4 v100, v86, 1.0 op_sel:[0,1,0]
	v_cvt_scalef32_pk_bf16_fp4 v101, v86, 1.0 op_sel:[1,1,0]
	v_mfma_f32_16x16x32_bf16 v[130:133], v[46:49], v[102:105], v[130:133]
	v_cvt_scalef32_pk_bf16_fp4 v102, v87, 1.0
	v_cvt_scalef32_pk_bf16_fp4 v103, v87, 1.0 op_sel:[1,0,0]
	v_cvt_scalef32_pk_bf16_fp4 v104, v87, 1.0 op_sel:[0,1,0]
	v_cvt_scalef32_pk_bf16_fp4 v105, v87, 1.0 op_sel:[1,1,0]
	v_mfma_f32_16x16x32_bf16 v[130:133], v[50:53], v[98:101], v[130:133]
	v_cvt_scalef32_pk_bf16_fp4 v98, v88, 1.0
	v_cvt_scalef32_pk_bf16_fp4 v99, v88, 1.0 op_sel:[1,0,0]
	v_cvt_scalef32_pk_bf16_fp4 v100, v88, 1.0 op_sel:[0,1,0]
	v_cvt_scalef32_pk_bf16_fp4 v101, v88, 1.0 op_sel:[1,1,0]
	v_mfma_f32_16x16x32_bf16 v[130:133], v[54:57], v[102:105], v[130:133]
	v_cvt_scalef32_pk_bf16_fp4 v102, v89, 1.0
	v_cvt_scalef32_pk_bf16_fp4 v103, v89, 1.0 op_sel:[1,0,0]
	v_cvt_scalef32_pk_bf16_fp4 v104, v89, 1.0 op_sel:[0,1,0]
	v_cvt_scalef32_pk_bf16_fp4 v105, v89, 1.0 op_sel:[1,1,0]
	v_mfma_f32_16x16x32_bf16 v[130:133], v[58:61], v[98:101], v[130:133]
	v_mfma_f32_16x16x32_bf16 v[130:133], v[62:65], v[102:105], v[130:133]
	s_waitcnt vmcnt(12)
	ds_read_b128 v[82:85], v146
	ds_read_b128 v[86:89], v147
	s_waitcnt lgkmcnt(2)
	s_add_i32 m0, s38, 0x3800
	v_mad_u32_u16 v142, v69, v249, v144 op_sel:[1,0,0,0]
	global_load_lds_dwordx4 v142, s[10:11]
	s_add_i32 m0, s38, 0x3c00
	v_mad_u32_u16 v143, v73, v249, v145 op_sel:[1,0,0,0]
	global_load_lds_dwordx4 v143, s[10:11]
	v_cvt_scalef32_pk_bf16_fp4 v98, v90, 1.0
	v_cvt_scalef32_pk_bf16_fp4 v99, v90, 1.0 op_sel:[1,0,0]
	v_cvt_scalef32_pk_bf16_fp4 v100, v90, 1.0 op_sel:[0,1,0]
	v_cvt_scalef32_pk_bf16_fp4 v101, v90, 1.0 op_sel:[1,1,0]
	v_cvt_scalef32_pk_bf16_fp4 v102, v91, 1.0
	v_cvt_scalef32_pk_bf16_fp4 v103, v91, 1.0 op_sel:[1,0,0]
	v_cvt_scalef32_pk_bf16_fp4 v104, v91, 1.0 op_sel:[0,1,0]
	v_cvt_scalef32_pk_bf16_fp4 v105, v91, 1.0 op_sel:[1,1,0]
	v_mfma_f32_16x16x32_bf16 v[134:137], v[34:37], v[98:101], 0
	v_cvt_scalef32_pk_bf16_fp4 v98, v92, 1.0
	v_cvt_scalef32_pk_bf16_fp4 v99, v92, 1.0 op_sel:[1,0,0]
	v_cvt_scalef32_pk_bf16_fp4 v100, v92, 1.0 op_sel:[0,1,0]
	v_cvt_scalef32_pk_bf16_fp4 v101, v92, 1.0 op_sel:[1,1,0]
	v_mfma_f32_16x16x32_bf16 v[134:137], v[38:41], v[102:105], v[134:137]
	v_cvt_scalef32_pk_bf16_fp4 v102, v93, 1.0
	v_cvt_scalef32_pk_bf16_fp4 v103, v93, 1.0 op_sel:[1,0,0]
	v_cvt_scalef32_pk_bf16_fp4 v104, v93, 1.0 op_sel:[0,1,0]
	v_cvt_scalef32_pk_bf16_fp4 v105, v93, 1.0 op_sel:[1,1,0]
	v_mfma_f32_16x16x32_bf16 v[134:137], v[42:45], v[98:101], v[134:137]
	v_cvt_scalef32_pk_bf16_fp4 v98, v94, 1.0
	v_cvt_scalef32_pk_bf16_fp4 v99, v94, 1.0 op_sel:[1,0,0]
	v_cvt_scalef32_pk_bf16_fp4 v100, v94, 1.0 op_sel:[0,1,0]
	v_cvt_scalef32_pk_bf16_fp4 v101, v94, 1.0 op_sel:[1,1,0]
	v_mfma_f32_16x16x32_bf16 v[134:137], v[46:49], v[102:105], v[134:137]
	v_cvt_scalef32_pk_bf16_fp4 v102, v95, 1.0
	v_cvt_scalef32_pk_bf16_fp4 v103, v95, 1.0 op_sel:[1,0,0]
	v_cvt_scalef32_pk_bf16_fp4 v104, v95, 1.0 op_sel:[0,1,0]
	v_cvt_scalef32_pk_bf16_fp4 v105, v95, 1.0 op_sel:[1,1,0]
	v_mfma_f32_16x16x32_bf16 v[134:137], v[50:53], v[98:101], v[134:137]
	v_cvt_scalef32_pk_bf16_fp4 v98, v96, 1.0
	v_cvt_scalef32_pk_bf16_fp4 v99, v96, 1.0 op_sel:[1,0,0]
	v_cvt_scalef32_pk_bf16_fp4 v100, v96, 1.0 op_sel:[0,1,0]
	v_cvt_scalef32_pk_bf16_fp4 v101, v96, 1.0 op_sel:[1,1,0]
	v_mfma_f32_16x16x32_bf16 v[134:137], v[54:57], v[102:105], v[134:137]
	v_cvt_scalef32_pk_bf16_fp4 v102, v97, 1.0
	v_cvt_scalef32_pk_bf16_fp4 v103, v97, 1.0 op_sel:[1,0,0]
	v_cvt_scalef32_pk_bf16_fp4 v104, v97, 1.0 op_sel:[0,1,0]
	v_cvt_scalef32_pk_bf16_fp4 v105, v97, 1.0 op_sel:[1,1,0]
	v_mfma_f32_16x16x32_bf16 v[134:137], v[58:61], v[98:101], v[134:137]
	v_cvt_pk_bf16_f32 v140, v122, v126
	v_mfma_f32_16x16x32_bf16 v[134:137], v[62:65], v[102:105], v[134:137]
	s_nop 7
	s_nop 7
	v_cvt_pk_bf16_f32 v141, v130, v134
	s_mov_b64 exec, 0xffff
	global_store_dwordx4 v151, v[138:141], s[4:5]
	s_mov_b64 exec, -1
	v_add_u32_e32 v151, s42, v151
	s_add_i32 s34, s34, 2
	s_cmp_lt_u32 s34, 8
	s_cbranch_scc1 .Le1_loop
	s_cmp_lt_i32 s35, 0
	s_cbranch_scc1 .Le1_exit
	s_add_i32 s39, s39, s43
	s_add_i32 s39, s39, 7
	s_mov_b32 s34, 0
	s_branch .Le1_loop
.Le1_exit:
	s_waitcnt vmcnt(0) lgkmcnt(0)
	s_branch .LBB0_722
